# conversion slot behind G4(0) tail: 13000 layer-1 weight items moved out of MODUL(1) into the idle last round of G4(0) via shared general conversion block
# baseline (speedup 1.0000x reference)
.LBB0_160:
	v_readlane_b32 s0, v251, 11
	v_readlane_b32 s1, v251, 12
	s_and_b64 s[0:1], s[0:1], s[2:3]
	s_andn2_b64 vcc, exec, s[0:1]
	s_cbranch_vccnz .LBB0_201
	v_readlane_b32 s0, v251, 13
	s_add_i32 s0, s25, s0
	s_cmp_gt_i32 s0, 0xc0f7
	s_waitcnt lgkmcnt(0)
	s_barrier
	s_cbranch_scc1 .LBB0_201
	s_add_u32 s28, s14, 0x5800000
	s_addc_u32 s29, s15, 0
	s_add_u32 s30, s34, 0x19a00000
	s_mulk_i32 s25, 0x2200
	s_waitcnt vmcnt(0)
	v_and_b32_e32 v11, 7, v145
	s_addc_u32 s31, s35, 0
	s_add_i32 s2, s0, 0x4268
	s_add_i32 s0, s25, 0
	v_lshrrev_b32_e32 v13, 3, v144
	v_lshlrev_b32_e32 v0, 4, v11
	v_add_u32_e32 v3, s0, v0
	s_waitcnt vmcnt(0)
	v_mul_u32_u24_e32 v7, 0x420, v11
	v_lshl_add_u64 v[22:23], s[14:15], 0, v[0:1]
	v_lshlrev_b32_e32 v0, 2, v13
	v_add3_u32 v7, s0, v7, v0
	s_movk_i32 s0, 0xb00
	v_mov_b32_e32 v0, 0x16000
	v_mad_u32_u24 v46, v13, s0, v0
	v_mov_b32_e32 v0, 0x1b800
	v_mad_u32_u24 v48, v13, s0, v0
	v_mov_b32_e32 v0, 0x21000
	v_mad_u32_u24 v50, v13, s0, v0
	v_mov_b32_e32 v0, 0x26800
	v_mad_u32_u24 v52, v13, s0, v0
	v_lshlrev_b32_e32 v0, 1, v11
	v_lshl_add_u64 v[32:33], s[14:15], 0, v[0:1]
	s_mov_b64 s[0:1], 0x5d00000
	v_lshl_add_u64 v[32:33], v[32:33], 0, s[0:1]
	s_mov_b64 s[0:1], 0x5e00000
	v_lshlrev_b32_e32 v2, 2, v11
	v_lshlrev_b32_e32 v20, 3, v11
	v_lshl_add_u64 v[34:35], v[22:23], 0, s[0:1]
	s_movk_i32 s0, 0x9a0
	v_mov_b32_e32 v11, 0x13400
	v_mad_u32_u24 v56, v13, s0, v11
	v_mov_b32_e32 v11, 0x18100
	s_add_u32 s22, s22, 0x40000
	v_lshlrev_b32_e32 v42, 2, v144
	v_mad_u32_u24 v58, v13, s0, v11
	v_mov_b32_e32 v11, 0x1ce00
	s_addc_u32 s23, s23, 0
	v_mov_b32_e32 v43, v1
	v_mad_u32_u24 v60, v13, s0, v11
	v_mov_b32_e32 v11, 0x21b00
	v_lshl_add_u64 v[40:41], s[16:17], 0, v[42:43]
	s_add_u32 s16, s26, 0x400000
	v_or_b32_e32 v9, 8, v13
	v_or_b32_e32 v15, 16, v13
	v_mad_u32_u24 v62, v13, s0, v11
	v_lshlrev_b32_e32 v11, 3, v144
	s_addc_u32 s17, s27, 0
	v_lshlrev_b32_e32 v4, 10, v13
	v_lshlrev_b32_e32 v6, 10, v9
	v_lshlrev_b32_e32 v8, 10, v15
	v_or_b32_e32 v17, 24, v13
	v_mul_u32_u24_e32 v5, 0x84, v13
	v_lshlrev_b32_e32 v24, 6, v13
	v_lshlrev_b32_e32 v26, 6, v9
	v_lshlrev_b32_e32 v28, 6, v15
	v_mul_u32_u24_e32 v44, 0xb00, v13
	v_and_b32_e32 v9, 32, v42
	v_mul_u32_u24_e32 v0, 0x9a0, v13
	v_and_b32_e32 v64, 0x1c0, v11
	v_lshrrev_b32_e32 v13, 4, v144
	v_or_b32_e32 v31, 64, v144
	s_movk_i32 s0, 0x180
	v_mov_b32_e32 v15, 0x6000
	v_or_b32_e32 v21, 0x80, v144
	v_mov_b32_e32 v19, 0xc000
	v_or_b32_e32 v27, 0xc0, v144
	v_lshl_add_u64 v[42:43], s[20:21], 0, v[42:43]
	s_add_u32 s20, s6, 0x9a0000
	v_lshlrev_b32_e32 v10, 10, v17
	v_or_b32_e32 v12, 0x8000, v4
	v_or_b32_e32 v14, 0xa000, v4
	v_or_b32_e32 v16, 0xc000, v4
	v_or_b32_e32 v18, 0xe000, v4
	v_lshlrev_b32_e32 v30, 6, v17
	v_mul_u32_u24_e32 v11, 0x180, v144
	v_mad_u32_u24 v15, v144, s0, v15
	v_lshrrev_b32_e32 v17, 4, v31
	v_mad_u32_u24 v19, v144, s0, v19
	v_lshrrev_b32_e32 v21, 4, v21
	v_mad_u32_u24 v25, v144, s0, v226
	v_lshrrev_b32_e32 v27, 4, v27
	v_lshlrev_b32_e32 v36, 11, v144
	v_mov_b32_e32 v37, v1
	v_or_b32_e32 v29, 16, v13
	v_lshlrev_b32_e32 v38, 11, v31
	v_mov_b32_e32 v39, v1
	v_or_b32_e32 v31, 20, v13
	s_addc_u32 s21, s7, 0
	s_lshl_b32 s25, s2, 5
	s_lshl_b32 s26, s71, 5
	v_lshlrev_b32_e32 v44, 2, v44
	v_lshlrev_b32_e32 v46, 2, v46
	v_lshlrev_b32_e32 v48, 2, v48
	v_lshlrev_b32_e32 v50, 2, v50
	v_lshlrev_b32_e32 v52, 2, v52
	v_lshlrev_b32_e32 v54, 2, v0
	v_lshlrev_b32_e32 v56, 2, v56
	v_lshlrev_b32_e32 v58, 2, v58
	v_lshlrev_b32_e32 v60, 2, v60
	v_lshlrev_b32_e32 v62, 2, v62
	v_lshlrev_b32_e32 v64, 1, v64
	s_branch .LBB0_164

.LBB0_1104:
	s_waitcnt vmcnt(0)
	s_barrier
	s_cmp_lg_u32 s24, 0
	s_cbranch_scc1 .Lcv_g4_skip
	v_readlane_b32 s56, v251, 2
	s_nop 0
	s_sub_i32 s56, s56, 8
	s_lshl_b32 s56, s56, 3
	s_cmp_lt_i32 s56, 0
	s_cbranch_scc1 .Lcv_g4_skip
	s_sub_i32 s59, s70, 8
	s_lshl_b32 s59, s59, 3
	s_mov_b32 s57, 0x32c8
	s_mov_b32 s58, 0xfa0
	s_mov_b32 s60, 0x4268
	s_mov_b32 s61, 1
	s_mov_b32 s62, s9
	s_mov_b32 s63, s13
	s_mov_b32 s64, s24
	s_mov_b32 s65, s55
	s_mov_b32 s66, s54
	s_mov_b32 s67, s52
	s_mov_b32 s68, s53
	v_readlane_b32 s0, v251, 8
	v_readlane_b32 s1, v251, 9
	s_nop 0
	s_load_dwordx2 s[2:3], s[0:1], 0x40
	s_load_dwordx4 s[4:7], s[0:1], 0x60
	s_load_dwordx8 s[12:19], s[0:1], 0xd8
	s_load_dwordx2 s[20:21], s[0:1], 0xc8
	s_load_dwordx4 s[24:27], s[0:1], 0x78
	s_load_dwordx2 s[28:29], s[0:1], 0xf8
	v_mbcnt_lo_u32_b32 v75, -1, 0
	v_mbcnt_hi_u32_b32 v75, -1, v75
	v_readlane_b32 s30, v251, 4
	v_and_b32_e32 v74, 63, v75
	s_waitcnt lgkmcnt(0)
	v_writelane_b32 v253, s2, 19
	s_nop 1
	v_writelane_b32 v253, s3, 20
	s_nop 1
	v_writelane_b32 v253, s4, 21
	s_nop 1
	v_writelane_b32 v253, s5, 22
	s_nop 1
	v_writelane_b32 v253, s6, 23
	s_nop 1
	v_writelane_b32 v253, s7, 24
	s_nop 1
	v_writelane_b32 v253, s24, 25
	s_nop 1
	v_writelane_b32 v253, s25, 26
	s_nop 1
	v_writelane_b32 v253, s26, 27
	s_nop 1
	v_writelane_b32 v253, s27, 28
	s_nop 1
	v_writelane_b32 v253, s20, 29
	s_nop 1
	v_writelane_b32 v253, s21, 30
	s_nop 1
	v_writelane_b32 v253, s28, 31
	s_nop 1
	v_writelane_b32 v253, s29, 32
	s_nop 1
	v_writelane_b32 v253, s12, 33
	s_nop 1
	v_writelane_b32 v253, s13, 34
	s_nop 1
	v_writelane_b32 v253, s14, 35
	s_nop 1
	v_writelane_b32 v253, s15, 36
	s_nop 1
	v_writelane_b32 v253, s16, 37
	s_nop 1
	v_writelane_b32 v253, s17, 38
	s_nop 1
	v_writelane_b32 v253, s18, 39
	s_nop 1
	v_writelane_b32 v253, s19, 40
	s_nop 1
	v_add_u32_e32 v10, s30, v75
	s_nop 0
	v_readfirstlane_b32 s0, v10
	s_ashr_i32 s0, s0, 6
	s_nop 0
	v_writelane_b32 v253, s0, 41
	s_nop 1
	s_branch .Lcv_entry
.Lcv_ret_g4:
	s_mov_b32 s9, s62
	s_mov_b32 s13, s63
	s_mov_b32 s24, s64
	s_mov_b32 s55, s65
	s_mov_b32 s54, s66
	s_mov_b32 s52, s67
	s_mov_b32 s53, s68
	s_mov_b32 s61, 0
.Lcv_g4_skip:
.LBB0_1105:
	s_mul_i32 s0, s24, 11
	s_add_i32 s16, s0, 8
	s_cmp_ge_i32 s16, s93
	s_cbranch_scc1 .LBB0_1117
	v_mbcnt_lo_u32_b32 v0, -1, 0
	v_mbcnt_hi_u32_b32 v0, -1, v0
	s_waitcnt vmcnt(0)
	v_readlane_b32 s0, v251, 4
	v_sub_u32_e32 v0, 0, v0
	s_nop 0
	v_cmp_eq_u32_e32 vcc, s0, v0
	s_barrier
	s_and_saveexec_b64 s[0:1], vcc
	s_movk_i32 s54, 0x6000
	s_cbranch_execz .LBB0_1159
	v_readlane_b32 s2, v253, 5
	s_waitcnt vmcnt(0) expcnt(0) lgkmcnt(0)
	s_nop 0
	v_mov_b32_e32 v0, s2
	ds_read_b32 v3, v0
	v_readlane_b32 s2, v253, 6
	s_waitcnt lgkmcnt(0)
	v_cmp_ne_u32_e32 vcc, 0, v3
	v_mov_b32_e32 v0, s2
	ds_read_b32 v2, v0
	s_cbranch_vccnz .LBB0_1123
	v_readlane_b32 s4, v251, 0
	v_readlane_b32 s5, v251, 1
	s_load_dwordx2 s[2:3], s[4:5], 0x4
	s_mov_b32 s9, 1
	s_waitcnt lgkmcnt(0)
	s_mul_i32 s8, s2, s70
	s_mul_i32 s8, s8, s3
	s_branch .LBB0_1110

.LBB0_1588:
	s_mov_b32 s61, 0
	v_readlane_b32 s2, v253, 17
	v_readlane_b32 s3, v253, 18
	s_mov_b64 s[0:1], -1
	s_and_b64 vcc, exec, s[2:3]
	v_readlane_b32 s55, v251, 2
	s_cbranch_vccz .LBB0_1631
	v_readlane_b32 s0, v252, 56
	v_readlane_b32 s1, v252, 57
	s_andn2_b64 vcc, exec, s[0:1]
	s_cbranch_vccnz .LBB0_1630
	v_readlane_b32 s56, v252, 58
	s_movk_i32 s57, 0xfa0
	s_mov_b32 s58, 0x10360
	v_readlane_b32 s59, v252, 59
	s_mov_b32 s60, 0x11300
.Lcv_entry:
	s_mov_b32 s0, s56
	v_readlane_b32 s1, v253, 41
	s_add_i32 s0, s0, s1
	s_cmp_ge_i32 s0, s57
	s_barrier
	s_cbranch_scc1 .LBB0_1630
	v_readlane_b32 s8, v253, 33
	v_readlane_b32 s10, v253, 35
	v_readlane_b32 s14, v253, 39
	v_readlane_b32 s11, v253, 36
	v_readlane_b32 s15, v253, 40
	s_add_u32 s10, s14, 0x5800000
	v_readlane_b32 s12, v253, 37
	s_addc_u32 s11, s15, 0
	v_readlane_b32 s2, v253, 31
	v_readlane_b32 s13, v253, 38
	v_readlane_b32 s3, v253, 32
	s_add_u32 s12, s2, 0x19a00000
	s_addc_u32 s13, s3, 0
	s_add_i32 s2, s0, s58
	v_readlane_b32 s0, v253, 41
	s_mulk_i32 s0, 0x2200
	v_and_b32_e32 v11, 7, v75
	s_add_i32 s0, s0, 0
	v_lshrrev_b32_e32 v13, 3, v74
	v_lshlrev_b32_e32 v0, 4, v11
	v_add_u32_e32 v3, s0, v0
	v_mul_u32_u24_e32 v7, 0x420, v11
	v_lshl_add_u64 v[22:23], s[14:15], 0, v[0:1]
	v_lshlrev_b32_e32 v0, 2, v13
	v_add3_u32 v7, s0, v7, v0
	s_movk_i32 s0, 0xb00
	v_mov_b32_e32 v0, 0x16000
	v_mad_u32_u24 v46, v13, s0, v0
	v_mov_b32_e32 v0, 0x1b800
	v_mad_u32_u24 v48, v13, s0, v0
	v_mov_b32_e32 v0, 0x21000
	v_mad_u32_u24 v50, v13, s0, v0
	v_mov_b32_e32 v0, 0x26800
	v_mad_u32_u24 v52, v13, s0, v0
	v_lshlrev_b32_e32 v0, 1, v11
	v_lshl_add_u64 v[32:33], s[14:15], 0, v[0:1]
	s_mov_b64 s[0:1], 0x5d00000
	v_lshl_add_u64 v[32:33], v[32:33], 0, s[0:1]
	s_mov_b64 s[0:1], 0x5e00000
	v_lshlrev_b32_e32 v2, 2, v11
	v_lshlrev_b32_e32 v20, 3, v11
	v_lshl_add_u64 v[34:35], v[22:23], 0, s[0:1]
	s_movk_i32 s0, 0x9a0
	v_mov_b32_e32 v11, 0x13400
	v_mad_u32_u24 v56, v13, s0, v11
	v_mov_b32_e32 v11, 0x18100
	v_mad_u32_u24 v58, v13, s0, v11
	v_mov_b32_e32 v11, 0x1ce00
	v_readlane_b32 s16, v253, 25
	v_or_b32_e32 v15, 16, v13
	v_mad_u32_u24 v60, v13, s0, v11
	v_mov_b32_e32 v11, 0x21b00
	v_readlane_b32 s18, v253, 27
	v_lshlrev_b32_e32 v8, 10, v15
	v_lshlrev_b32_e32 v28, 6, v15
	v_mad_u32_u24 v62, v13, s0, v11
	s_movk_i32 s0, 0x180
	v_mov_b32_e32 v15, 0x6000
	v_mov_b32_e32 v19, 0xc000
	v_readlane_b32 s19, v253, 28
	s_add_u32 s14, s18, 0x40000
	v_readlane_b32 s4, v253, 21
	v_or_b32_e32 v9, 8, v13
	v_lshlrev_b32_e32 v42, 2, v74
	v_mad_u32_u24 v15, v74, s0, v15
	v_mad_u32_u24 v19, v74, s0, v19
	v_mad_u32_u24 v25, v74, s0, v226
	v_readlane_b32 s17, v253, 26
	s_addc_u32 s15, s19, 0
	v_mov_b32_e32 v43, v1
	v_readlane_b32 s5, v253, 22
	v_readlane_b32 s0, v253, 29
	v_lshlrev_b32_e32 v6, 10, v9
	v_lshlrev_b32_e32 v26, 6, v9
	v_and_b32_e32 v9, 32, v42
	v_lshl_add_u64 v[40:41], s[4:5], 0, v[42:43]
	v_lshl_add_u64 v[42:43], s[16:17], 0, v[42:43]
	v_readlane_b32 s1, v253, 30
	s_add_u32 s16, s0, 0x400000
	v_lshlrev_b32_e32 v11, 3, v74
	s_addc_u32 s17, s1, 0
	v_readlane_b32 s0, v253, 19
	v_lshlrev_b32_e32 v4, 10, v13
	v_or_b32_e32 v17, 24, v13
	v_mul_u32_u24_e32 v5, 0x84, v13
	v_lshlrev_b32_e32 v24, 6, v13
	v_mul_u32_u24_e32 v44, 0xb00, v13
	v_mul_u32_u24_e32 v0, 0x9a0, v13
	v_and_b32_e32 v64, 0x1c0, v11
	v_lshrrev_b32_e32 v13, 4, v74
	v_or_b32_e32 v31, 64, v74
	v_or_b32_e32 v21, 0x80, v74
	v_or_b32_e32 v27, 0xc0, v74
	v_readlane_b32 s1, v253, 20
	s_add_u32 s18, s0, 0x9a0000
	s_mov_b32 s0, s59
	v_lshlrev_b32_e32 v10, 10, v17
	v_or_b32_e32 v12, 0x8000, v4
	v_or_b32_e32 v14, 0xa000, v4
	v_or_b32_e32 v16, 0xc000, v4
	v_or_b32_e32 v18, 0xe000, v4
	v_lshlrev_b32_e32 v30, 6, v17
	v_mul_u32_u24_e32 v11, 0x180, v74
	v_lshrrev_b32_e32 v17, 4, v31
	v_lshrrev_b32_e32 v21, 4, v21
	v_lshrrev_b32_e32 v27, 4, v27
	v_lshlrev_b32_e32 v36, 11, v74
	v_mov_b32_e32 v37, v1
	v_or_b32_e32 v29, 16, v13
	v_lshlrev_b32_e32 v38, 11, v31
	v_mov_b32_e32 v39, v1
	v_or_b32_e32 v31, 20, v13
	s_addc_u32 s19, s1, 0
	s_lshl_b32 s20, s2, 5
	s_lshl_b32 s21, s0, 5
	v_lshlrev_b32_e32 v44, 2, v44
	v_lshlrev_b32_e32 v46, 2, v46
	v_lshlrev_b32_e32 v48, 2, v48
	v_lshlrev_b32_e32 v50, 2, v50
	v_lshlrev_b32_e32 v52, 2, v52
	v_lshlrev_b32_e32 v54, 2, v0
	v_lshlrev_b32_e32 v56, 2, v56
	v_lshlrev_b32_e32 v58, 2, v58
	v_lshlrev_b32_e32 v60, 2, v60
	v_lshlrev_b32_e32 v62, 2, v62
	v_lshlrev_b32_e32 v64, 1, v64
	v_readlane_b32 s9, v253, 34
	v_readlane_b32 s6, v253, 23
	v_readlane_b32 s7, v253, 24
	s_branch .LBB0_1593
.LBB0_1592:
	s_mov_b32 s0, s59
	s_add_i32 s2, s2, s0
	s_add_i32 s20, s20, s21
	s_cmp_lt_i32 s2, s60
	s_cbranch_scc0 .LBB0_1630

.LBB0_1630:
	s_cmp_eq_u32 s61, 0
	s_cbranch_scc1 .Lcv_exit_topk
	s_branch .Lcv_ret_g4
